# scan C progress polls: s_sleep 24 -> 8 between polls
# baseline (speedup 1.0000x reference)
; #define GAS __attribute__((address_space(1)))
; DI void scanc_load(ScanCIn& o, const unsigned char* ws, GAS unsigned* flags, int item, int r16, int g, int l) {
;     ...
;       GAS unsigned* fw = flags + 64 * bh; const unsigned need = 4u * ((unsigned)(c >> 2) + 1u); unsigned spins = 0;
;       while ((unsigned)__builtin_amdgcn_readfirstlane((int)__hip_atomic_load(fw, __ATOMIC_RELAXED, __HIP_MEMORY_SCOPE_AGENT)) < need) { __builtin_amdgcn_s_sleep(24); if (++spins > (1u << 20)) break; }
.LBB0_1229:
	s_cmp_lg_u32 s99, s12
	s_cselect_b32 s98, 0, s98
	s_mov_b32 s99, s12
	s_cmp_ge_u32 s98, s6
	s_mov_b64 s[2:3], -1
	s_cbranch_scc1 .LBB0_1228
	global_load_dword v0, v65, s[0:1] sc1
	s_waitcnt vmcnt(0)
	v_readfirstlane_b32 s2, v0
	s_mov_b32 s98, s2
	s_cmp_ge_u32 s2, s6
	s_mov_b64 s[2:3], -1
	s_cbranch_scc1 .LBB0_1228
	s_add_i32 s7, s7, -1
	s_cmp_eq_u32 s7, 0
	s_cselect_b64 s[2:3], -1, 0
	s_sleep 8
	s_branch .LBB0_1228

; #define GAS __attribute__((address_space(1)))
; DI void scanc_load(ScanCIn& o, const unsigned char* ws, GAS unsigned* flags, int item, int r16, int g, int l) {
;     ...
;       GAS unsigned* fw = flags + 64 * bh; const unsigned need = 4u * ((unsigned)(c >> 2) + 1u); unsigned spins = 0;
;       while ((unsigned)__builtin_amdgcn_readfirstlane((int)__hip_atomic_load(fw, __ATOMIC_RELAXED, __HIP_MEMORY_SCOPE_AGENT)) < need) { __builtin_amdgcn_s_sleep(24); if (++spins > (1u << 20)) break; }
.LBB0_1238:
	s_cmp_lg_u32 s99, s28
	s_cselect_b32 s98, 0, s98
	s_mov_b32 s99, s28
	s_cmp_ge_u32 s98, s30
	s_mov_b64 s[16:17], -1
	s_cbranch_scc1 .LBB0_1237
	global_load_dword v16, v65, s[14:15] sc1
	s_waitcnt vmcnt(0)
	v_readfirstlane_b32 s16, v16
	s_mov_b32 s98, s16
	s_cmp_ge_u32 s16, s30
	s_mov_b64 s[16:17], -1
	s_cbranch_scc1 .LBB0_1237
	s_add_i32 s31, s31, -1
	s_cmp_eq_u32 s31, 0
	s_cselect_b64 s[16:17], -1, 0
	s_sleep 8
	s_branch .LBB0_1237

; #define GAS __attribute__((address_space(1)))
; DI void scanc_load(ScanCIn& o, const unsigned char* ws, GAS unsigned* flags, int item, int r16, int g, int l) {
;     ...
;       GAS unsigned* fw = flags + 64 * bh; const unsigned need = 4u * ((unsigned)(c >> 2) + 1u); unsigned spins = 0;
;       while ((unsigned)__builtin_amdgcn_readfirstlane((int)__hip_atomic_load(fw, __ATOMIC_RELAXED, __HIP_MEMORY_SCOPE_AGENT)) < need) { __builtin_amdgcn_s_sleep(24); if (++spins > (1u << 20)) break; }
.LBB0_1245:
	s_cmp_lg_u32 s99, s26
	s_cselect_b32 s98, 0, s98
	s_mov_b32 s99, s26
	s_cmp_ge_u32 s98, s28
	s_mov_b64 s[14:15], -1
	s_cbranch_scc1 .LBB0_1244
	global_load_dword v0, v65, s[12:13] sc1
	s_waitcnt vmcnt(0)
	v_readfirstlane_b32 s14, v0
	s_mov_b32 s98, s14
	s_cmp_ge_u32 s14, s28
	s_mov_b64 s[14:15], -1
	s_cbranch_scc1 .LBB0_1244
	s_add_i32 s29, s29, -1
	s_cmp_eq_u32 s29, 0
	s_cselect_b64 s[14:15], -1, 0
	s_sleep 8
	s_branch .LBB0_1244
